# adds entry-point warm-up drivers so the k_layer<1>/<2> prologues are also fetched 16-wide
# speedup vs baseline: 1.2990x; 1.0100x over previous
_Z7k_layerILi1EEvPKDF16_PKiPKjS3_S3_S1_PKfPDF16_PhS3_S7_Pf:
	v_readfirstlane_b32 s3, v0
	s_lshr_b32 s3, s3, 6
	s_cmp_eq_u32 s3, 0
	s_cbranch_scc1 .Lic1p_t0
	s_cmp_eq_u32 s3, 1
	s_cbranch_scc1 .Lic1p_t1
	s_cmp_eq_u32 s3, 2
	s_cbranch_scc1 .Lic1p_t2
	s_cmp_eq_u32 s3, 3
	s_cbranch_scc1 .Lic1p_t3
	s_cmp_eq_u32 s3, 4
	s_cbranch_scc1 .Lic1p_t4
	s_cmp_eq_u32 s3, 5
	s_cbranch_scc1 .Lic1p_t5
	s_cmp_eq_u32 s3, 6
	s_cbranch_scc1 .Lic1p_t6
	s_cmp_eq_u32 s3, 7
	s_cbranch_scc1 .Lic1p_t7
	s_cmp_eq_u32 s3, 8
	s_cbranch_scc1 .Lic1p_t8
	s_cmp_eq_u32 s3, 9
	s_cbranch_scc1 .Lic1p_t9
.Lic1p_done:
	s_load_dwordx2 s[24:25], s[0:1], 0x50
	s_load_dwordx8 s[8:15], s[0:1], 0x0
	s_load_dwordx8 s[16:23], s[0:1], 0x20
	v_lshrrev_b32_e32 v2, 5, v0
	v_and_b32_e32 v4, 31, v0
	v_mul_u32_u24_e32 v3, 0x220, v2
	v_lshlrev_b32_e32 v5, 4, v4
	v_or_b32_e32 v1, 0xfffffc00, v0
	v_add3_u32 v4, v3, v5, 0
	v_add_u32_e32 v4, 0x1cd90, v4
	v_lshl_or_b32 v2, v2, 9, v5
	v_mov_b32_e32 v3, 0
	s_branch .Lic1p_s0

.Lic1p_s0:
	s_waitcnt lgkmcnt(0)
	v_add_u32_e32 v3, 0x4000, v2
	v_lshlrev_b32_e32 v30, 4, v0
	v_cmp_gt_u32_e64 s[34:35], 16, v0
	v_lshrrev_b32_e32 v39, 6, v0
	s_and_saveexec_b64 s[4:5], s[34:35]
	global_load_dwordx4 v[42:45], v30, s[20:21]
	s_mov_b64 exec, s[4:5]
	global_load_dwordx4 v[6:9], v2, s[18:19]
	global_load_dwordx4 v[10:13], v3, s[18:19]
	v_add_u32_e32 v31, 0x4000, v30
	v_add_u32_e32 v32, 0x8000, v30
	s_branch .Lic1p_s1

.Lic1p_s1:
	v_add_u32_e32 v33, 0xc000, v30
	global_load_dwordx4 v[14:17], v30, s[8:9]
	global_load_dwordx4 v[18:21], v31, s[8:9]
	global_load_dwordx4 v[22:25], v32, s[8:9]
	global_load_dwordx4 v[26:29], v33, s[8:9]
	v_readfirstlane_b32 s36, v39
	v_mov_b32_e32 v40, v4
	v_add_u32_e32 v41, 0xcc10, v30
	v_add_u32_e32 v38, 0x1cc90, v30
	v_cmp_gt_u32_e32 vcc, 64, v0
	s_and_saveexec_b64 s[4:5], vcc
	v_lshl_add_u32 v1, v0, 1, 0
	s_branch .Lic1p_s2

.Lic1p_s2:
	v_add_u32_e32 v1, 0x1cc10, v1
	v_mov_b32_e32 v2, 0
	ds_write_b16 v1, v2
	s_mov_b64 exec, s[4:5]
	v_cmp_eq_u32_e32 vcc, 0, v0
	s_and_saveexec_b64 s[4:5], vcc
	v_mov_b32_e32 v1, 0
	v_mov_b32_e32 v2, 16
	ds_write_b32 v1, v2 offset:52224
	s_mov_b64 exec, s[4:5]
	s_mul_i32 s8, s2, 0x186a0
	s_lshr_b32 s8, s8, 8
	s_branch .Lic1p_s3

.Lic1p_s3:
	s_add_i32 s3, s2, 1
	s_mul_i32 s18, s3, 0x186a0
	s_lshr_b32 s18, s18, 8
.LBB4_14:
	v_lshrrev_b32_e32 v2, 3, v0
	s_load_dwordx2 s[4:5], s[0:1], 0x40
	v_and_b32_e32 v2, 0x78, v2
	s_movk_i32 s2, 0xa0
	v_and_b32_e32 v97, 7, v0
	s_sub_i32 s0, s18, s8
	v_and_b32_e32 v1, 63, v0
	v_mov_b32_e32 v89, 0
	v_mad_u32_u24 v3, v2, s2, 0
	s_branch .Lic1p_s4

.Lic1p_s4:
	v_bfe_u32 v96, v0, 3, 3
	v_and_b32_e32 v99, 15, v0
	v_bfe_u32 v4, v0, 4, 2
	s_add_i32 s0, s0, 7
	v_mul_u32_u24_e32 v5, 0xa0, v97
	v_and_b32_e32 v0, 48, v0
	s_ashr_i32 s9, s0, 3
	v_cmp_eq_u32_e64 s[0:1], 0, v1
	v_mad_u32_u24 v1, v96, s2, v3
	v_lshlrev_b32_e32 v2, 3, v4
	v_add3_u32 v103, v3, v5, v0
	v_mov_b32_e32 v3, v89
	s_branch .Lic1p_s5

.Lic1p_s5:
	v_lshlrev_b32_e32 v98, 4, v97
	v_add_u32_e32 v0, 0, v0
	v_lshlrev_b32_e32 v88, 2, v4
	v_lshl_add_u64 v[90:91], s[22:23], 0, v[2:3]
	v_mul_u32_u24_e32 v2, 0x220, v99
	v_or_b32_e32 v100, 8, v97
	v_or_b32_e32 v101, 16, v97
	v_add_u32_e32 v102, 0, v98
	v_cmp_gt_u32_e64 s[2:3], 8, v99
	s_waitcnt lgkmcnt(0)
	v_lshl_add_u64 v[92:93], s[4:5], 0, v[88:89]
	v_lshlrev_b32_e32 v88, 2, v88
	s_branch .Lic1p_s6

.Lic1p_s6:
	v_add_u32_e32 v104, v1, v98
	v_add_u32_e32 v105, v0, v2
	v_add_u32_e32 v105, 0x1cd90, v105
	s_lshl_b32 s19, s36, 3
	s_add_i32 s19, s19, s8
	v_add_u32_e32 v94, s19, v96
	v_cmp_gt_i32_e64 s[4:5], s18, v94
	v_mov_b32_e32 v32, 0
	v_mov_b32_e32 v33, 0
	v_mov_b32_e32 v34, 0
	v_mov_b32_e32 v35, 0
	s_and_saveexec_b64 s[6:7], s[4:5]
	s_branch .Lic1p_s7

.Lic1p_s7:
	v_lshl_add_u32 v36, v94, 1, v94
	v_lshlrev_b32_e32 v36, 2, v36
	global_load_dwordx4 v[32:35], v36, s[10:11]
	s_mov_b64 exec, s[6:7]
	s_cmp_eq_u32 s36, 0
	s_cbranch_scc1 .Lic1_t0
	s_cmp_eq_u32 s36, 1
	s_cbranch_scc1 .Lic1_t1
	s_cmp_eq_u32 s36, 2
	s_cbranch_scc1 .Lic1_t2
	s_cmp_eq_u32 s36, 3
	s_cbranch_scc1 .Lic1_t3
	s_branch .Lic1p_s8

.Lic1p_s8:
	s_cmp_eq_u32 s36, 4
	s_cbranch_scc1 .Lic1_t4
	s_cmp_eq_u32 s36, 5
	s_cbranch_scc1 .Lic1_t5
	s_cmp_eq_u32 s36, 6
	s_cbranch_scc1 .Lic1_t6
	s_cmp_eq_u32 s36, 7
	s_cbranch_scc1 .Lic1_t7
	s_cmp_eq_u32 s36, 8
	s_cbranch_scc1 .Lic1_t8
	s_cmp_eq_u32 s36, 9
	s_cbranch_scc1 .Lic1_t9
	s_branch .Lic1p_s9

.Lic1p_s9:
	s_cmp_eq_u32 s36, 10
	s_cbranch_scc1 .Lic1_t10
	s_cmp_eq_u32 s36, 11
	s_cbranch_scc1 .Lic1_t11
	s_cmp_eq_u32 s36, 12
	s_cbranch_scc1 .Lic1_t12
	s_cmp_eq_u32 s36, 13
	s_cbranch_scc1 .Lic1_t13
	s_cmp_eq_u32 s36, 14
	s_cbranch_scc1 .Lic1_t14
	s_cmp_eq_u32 s36, 15
	s_cbranch_scc1 .Lic1_t15

_Z7k_layerILi2EEvPKDF16_PKiPKjS3_S3_S1_PKfPDF16_PhS3_S7_Pf:
	v_readfirstlane_b32 s3, v0
	s_lshr_b32 s3, s3, 6
	s_cmp_eq_u32 s3, 0
	s_cbranch_scc1 .Lic2p_t0
	s_cmp_eq_u32 s3, 1
	s_cbranch_scc1 .Lic2p_t1
	s_cmp_eq_u32 s3, 2
	s_cbranch_scc1 .Lic2p_t2
	s_cmp_eq_u32 s3, 3
	s_cbranch_scc1 .Lic2p_t3
	s_cmp_eq_u32 s3, 4
	s_cbranch_scc1 .Lic2p_t4
	s_cmp_eq_u32 s3, 5
	s_cbranch_scc1 .Lic2p_t5
	s_cmp_eq_u32 s3, 6
	s_cbranch_scc1 .Lic2p_t6
	s_cmp_eq_u32 s3, 7
	s_cbranch_scc1 .Lic2p_t7
	s_cmp_eq_u32 s3, 8
	s_cbranch_scc1 .Lic2p_t8
	s_cmp_eq_u32 s3, 9
	s_cbranch_scc1 .Lic2p_t9
.Lic2p_done:
	s_load_dwordx2 s[24:25], s[0:1], 0x58
	s_load_dwordx4 s[12:15], s[0:1], 0x0
	s_load_dwordx2 s[26:27], s[0:1], 0x10
	s_load_dwordx4 s[16:19], s[0:1], 0x48
	s_load_dwordx4 s[20:23], s[0:1], 0x28
	v_lshrrev_b32_e32 v2, 5, v0
	v_and_b32_e32 v4, 31, v0
	v_mul_u32_u24_e32 v3, 0x220, v2
	v_lshlrev_b32_e32 v5, 4, v4
	v_add3_u32 v4, v3, v5, 0
	v_add_u32_e32 v4, 0xcf10, v4
	v_lshl_or_b32 v2, v2, 9, v5
	s_branch .Lic2p_s0

.Lic2p_s0:
	v_mov_b32_e32 v3, 0
	v_or_b32_e32 v1, 0xfffffc00, v0
	s_waitcnt lgkmcnt(0)
	v_add_u32_e32 v3, 0x4000, v2
	v_lshlrev_b32_e32 v14, 4, v0
	v_add_u32_e32 v15, 0xffffff00, v14
	v_lshrrev_b32_e32 v21, 6, v0
	s_mov_b64 s[4:5], exec
	v_cmp_gt_u32_e32 vcc, 16, v0
	v_cmp_gt_u32_e64 s[40:41], 48, v0
	s_andn2_b64 s[8:9], s[40:41], vcc
	s_and_b64 exec, s[4:5], vcc
	s_branch .Lic2p_s1

.Lic2p_s1:
	global_load_dwordx4 v[16:19], v14, s[22:23]
	s_and_b64 exec, s[4:5], s[8:9]
	global_load_dwordx4 v[16:19], v15, s[18:19]
	s_mov_b64 exec, s[4:5]
	global_load_dwordx4 v[22:25], v2, s[20:21]
	global_load_dwordx4 v[26:29], v3, s[20:21]
	v_readfirstlane_b32 s38, v21
	v_mov_b32_e32 v20, v4
	v_cmp_eq_u32_e32 vcc, 0, v0
	s_and_saveexec_b64 s[6:7], vcc
	v_mov_b32_e32 v1, 0
	v_mov_b32_e32 v2, 16
	s_branch .Lic2p_s2

.Lic2p_s2:
	ds_write_b32 v1, v2 offset:52224
	s_mov_b64 exec, s[6:7]
	s_mul_i32 s20, s2, 0x186a0
	s_lshr_b32 s20, s20, 8
	s_add_i32 s3, s2, 1
	s_mul_i32 s28, s3, 0x186a0
	s_lshr_b32 s28, s28, 8
.LBB5_10:
	v_lshrrev_b32_e32 v2, 3, v0
	s_load_dwordx2 s[30:31], s[0:1], 0x40
	v_and_b32_e32 v1, 63, v0
	v_and_b32_e32 v2, 0x78, v2
	s_movk_i32 s2, 0xa0
	s_branch .Lic2p_s3

.Lic2p_s3:
	v_bfe_u32 v74, v0, 3, 3
	v_and_b32_e32 v75, 7, v0
	v_and_b32_e32 v77, 15, v0
	s_sub_i32 s0, s28, s20
	v_and_b32_e32 v5, 48, v0
	v_lshrrev_b32_e32 v0, 2, v0
	v_mad_u32_u24 v2, v2, s2, 0
	s_add_i32 s0, s0, 7
	v_mul_u32_u24_e32 v4, 0xa0, v75
	v_and_b32_e32 v0, 12, v0
	v_lshlrev_b32_e32 v76, 4, v75
	s_ashr_i32 s21, s0, 3
	s_branch .Lic2p_s4

.Lic2p_s4:
	v_cmp_eq_u32_e64 s[0:1], 0, v1
	v_mad_u32_u24 v3, v74, s2, v2
	v_add3_u32 v80, v2, v4, v5
	v_add_u32_e32 v2, 0, v5
	v_cmp_gt_u32_e64 s[4:5], 16, v1
	v_mul_u32_u24_e32 v1, 0x220, v77
	v_lshlrev_b32_e32 v32, 2, v0
	v_mbcnt_lo_u32_b32 v0, -1, 0
	v_mov_b32_e32 v33, 0
	v_or_b32_e32 v78, 8, v75
	v_or_b32_e32 v79, 16, v75
	v_lshlrev_b32_e32 v81, 3, v75
	s_branch .Lic2p_s5

.Lic2p_s5:
	v_cmp_gt_u32_e64 s[2:3], 8, v77
	s_mov_b32 s29, 0x3c800000
	v_add_u32_e32 v82, v3, v76
	v_add_u32_e32 v83, v2, v1
	v_add_u32_e32 v83, 0xcf10, v83
	v_mbcnt_hi_u32_b32 v84, -1, v0
	s_lshl_b32 s33, s38, 3
	s_add_i32 s33, s33, s20
	v_add_u32_e32 v8, s33, v74
	v_cmp_gt_i32_e32 vcc, s28, v8
	v_mov_b32_e32 v0, 0
	v_mov_b32_e32 v1, 0
	s_branch .Lic2p_s6

.Lic2p_s6:
	v_mov_b32_e32 v2, 0
	v_mov_b32_e32 v3, 0
	v_mov_b32_e32 v4, 0
	v_mov_b32_e32 v5, 0
	v_mov_b32_e32 v6, 0
	v_mov_b32_e32 v7, 0
	s_and_saveexec_b64 s[6:7], vcc
	v_lshl_add_u32 v9, v8, 1, v8
	v_lshlrev_b32_e32 v9, 2, v9
	global_load_dwordx4 v[4:7], v9, s[14:15]
	v_lshl_or_b32 v9, v8, 7, v76
	global_load_dwordx4 v[0:3], v9, s[12:13]
	s_branch .Lic2p_s7

.Lic2p_s7:
	s_mov_b64 exec, s[6:7]
	s_cmp_eq_u32 s38, 0
	s_cbranch_scc1 .Lic2_t0
	s_cmp_eq_u32 s38, 1
	s_cbranch_scc1 .Lic2_t1
	s_cmp_eq_u32 s38, 2
	s_cbranch_scc1 .Lic2_t2
	s_cmp_eq_u32 s38, 3
	s_cbranch_scc1 .Lic2_t3
	s_cmp_eq_u32 s38, 4
	s_cbranch_scc1 .Lic2_t4
	s_cmp_eq_u32 s38, 5
	s_branch .Lic2p_s8

.Lic2p_s8:
	s_cbranch_scc1 .Lic2_t5
	s_cmp_eq_u32 s38, 6
	s_cbranch_scc1 .Lic2_t6
	s_cmp_eq_u32 s38, 7
	s_cbranch_scc1 .Lic2_t7
	s_cmp_eq_u32 s38, 8
	s_cbranch_scc1 .Lic2_t8
	s_cmp_eq_u32 s38, 9
	s_cbranch_scc1 .Lic2_t9
	s_cmp_eq_u32 s38, 10
	s_cbranch_scc1 .Lic2_t10
	s_cmp_eq_u32 s38, 11
	s_branch .Lic2p_s9

.Lic2p_s9:
	s_cbranch_scc1 .Lic2_t11
	s_cmp_eq_u32 s38, 12
	s_cbranch_scc1 .Lic2_t12
	s_cmp_eq_u32 s38, 13
	s_cbranch_scc1 .Lic2_t13
	s_cmp_eq_u32 s38, 14
	s_cbranch_scc1 .Lic2_t14
	s_cmp_eq_u32 s38, 15
	s_cbranch_scc1 .Lic2_t15
